# v21 + the 7th (mostly empty) conversion slot reassigned to the workgroups that have slack before the down-projection barrier
# baseline (speedup 1.0000x reference)
; DI unsigned pk_bf16(float lo, float hi) { const f32x2 v = {lo, hi}; return __builtin_bit_cast(unsigned, __builtin_convertvector(v, bf16x2_t)); }
; DI float silu_mul(float g, float u) { return g * sigmoidf_(g) * u; }
; DI int pair_perm512(int n) { return ((n & 255) >> 7) * 256 + (n >> 8) * 128 + (n & 127); }
;     DI void operator()(const f32x4 (&acc)[2][2][4][2], const Unit& u, int wr, int wc, int fr, int fq) const {
;         const int col0 = u.pn * 128 + wc * 32 + 8 * fq;
;         float w8[2][4];
; #pragma unroll
;         for (int ai = 0; ai < 2; ++ai)
; #pragma unroll
;             for (int m = 0; m < 4; ++m) w8[ai][m] = (u.aux >= 0) ? roww[u.orow + ai * 128 + wr * 64 + m * 16 + fr] : 1.0f;
; #pragma unroll
;         for (int ai = 0; ai < 2; ++ai)
; #pragma unroll
;             for (int m = 0; m < 4; ++m) { const int row = u.orow + ai * 128 + wr * 64 + m * 16 + fr;
;                 bf16_t* rowp = ACT + (size_t)row * 256 + col0;
;                 float v[8];
; #pragma unroll
;                 for (int n = 0; n < 2; ++n)
; #pragma unroll
;                     for (int j = 0; j < 4; ++j) v[n * 4 + j] = silu_mul(acc[ai][0][m][n][j], acc[ai][1][m][n][j]) * w8[ai][m];
;                 u32x4 w; w.x = pk_bf16(v[0], v[1]); w.y = pk_bf16(v[2], v[3]); w.z = pk_bf16(v[4], v[5]); w.w = pk_bf16(v[6], v[7]);
;                 *(u32x4*)rowp = w; }
; DI void phase_prologue(const Ctx& c) {
;     ...
;         const int tk = jb.K / 64, tn = jb.N / 64, per = tk * tn, total = jb.count * per;
;         for (int t = gw; t < total; t += nw) {
;             const int mi = t / per, r = t % per, kt = r / tn, ntl = r % tn;
;             const float* src = jb.src + (size_t)mi * jb.K * jb.N;
;             const int n0 = ntl * 64; int drow = n0; float scale = 1.0f;
;             if (jb.mode == 1) drow = pair_perm512(n0);
;             if (jb.mode == 2 && n0 < 1024) scale = 0.125f;
;             bf16_t* dst = jb.dst + (size_t)mi * jb.K * jb.N + (size_t)drow * jb.K + kt * 64;
.LBB0_1239:
	v_mul_f32_e32 v135, 0xbfb8aa3b, v124
	v_exp_f32_e32 v135, v135
	v_mul_f32_e32 v141, 0xbfb8aa3b, v125
	v_exp_f32_e32 v141, v141
	v_mul_f32_e32 v143, 0xbfb8aa3b, v127
	v_add_f32_e32 v135, 1.0, v135
	v_rcp_f32_e32 v170, v135
	v_add_f32_e32 v135, 1.0, v141
	v_mul_f32_e32 v141, 0xbfb8aa3b, v126
	v_exp_f32_e32 v141, v141
	v_exp_f32_e32 v143, v143
	v_rcp_f32_e32 v171, v135
	v_lshl_or_b32 v168, s8, 7, v163
	v_add_f32_e32 v135, 1.0, v141
	v_rcp_f32_e32 v172, v135
	v_add_f32_e32 v135, 1.0, v143
	v_rcp_f32_e32 v173, v135
	v_pk_mul_f32 v[124:125], v[124:125], v[170:171]
	v_ashrrev_i32_e32 v169, 31, v168
	v_pk_mul_f32 v[120:121], v[124:125], v[120:121]
	v_pk_mul_f32 v[124:125], v[126:127], v[172:173]
	v_mul_f32_e32 v126, 0xbfb8aa3b, v118
	v_pk_mul_f32 v[122:123], v[124:125], v[122:123]
	v_mul_f32_e32 v124, 0xbfb8aa3b, v116
	v_mul_f32_e32 v125, 0xbfb8aa3b, v117
	v_exp_f32_e32 v124, v124
	v_exp_f32_e32 v125, v125
	v_mul_f32_e32 v127, 0xbfb8aa3b, v119
	v_exp_f32_e32 v126, v126
	v_exp_f32_e32 v127, v127
	v_add_f32_e32 v124, 1.0, v124
	v_add_f32_e32 v125, 1.0, v125
	v_rcp_f32_e32 v124, v124
	v_rcp_f32_e32 v125, v125
	v_add_f32_e32 v126, 1.0, v126
	v_add_f32_e32 v127, 1.0, v127
	v_rcp_f32_e32 v126, v126
	v_rcp_f32_e32 v127, v127
	v_pk_mul_f32 v[116:117], v[116:117], v[124:125]
	v_lshlrev_b64 v[152:153], 9, v[152:153]
	v_pk_mul_f32 v[112:113], v[116:117], v[112:113]
	v_lshl_add_u64 v[152:153], s[14:15], 0, v[152:153]
	s_waitcnt vmcnt(0)
	s_mov_b32 s85, 0
	s_cmp_gt_u32 s94, 2
	s_cbranch_scc1 .Lcv_ld_done
	v_readlane_b32 s74, v255, 3
	s_cmp_eq_u32 s9, 7
	s_cbranch_scc1 .Lcv_u6
	s_lshl_b32 s75, s96, 3
	s_add_i32 s74, s74, s75
	s_add_i32 s75, s9, -1
	s_lshl_b32 s75, s75, 11
	s_add_i32 s74, s74, s75
	s_branch .Lcv_tchk
.Lcv_u6:
	s_and_b32 s75, s96, 7
	s_cmp_lg_u32 s75, 2
	s_cbranch_scc1 .Lcv_ld_done
	s_and_b32 s75, s96, 0xfffffff8
	s_add_i32 s74, s74, s75
	s_addk_i32 s74, 0x3000
.Lcv_tchk:
	s_cmpk_gt_u32 s74, 0x30bf
	s_cbranch_scc1 .Lcv_ld_done
	s_load_dwordx2 s[76:77], s[92:93], 0xb8
	s_add_i32 s78, s94, 1
	s_cmpk_lt_u32 s74, 0x2000
	s_cbranch_scc1 .Lcv_gu
	s_cmpk_lt_u32 s74, 0x3000
	s_cbranch_scc1 .Lcv_dn
	s_cmpk_lt_u32 s74, 0x3080
	s_cbranch_scc1 .Lcv_sgu
	s_load_dwordx2 s[80:81], s[92:93], 0xa8
	s_sub_i32 s74, s74, 0x3080
	s_mov_b32 s79, s78
	s_mov_b32 s83, 0x19d40800
	s_branch .Lcv_dn_common
